# gather epilogue: counted waits, each reloaded x1 chunk of the second token is used as soon as it has landed
# baseline (speedup 1.0000x reference)
; DI void peer_token(LAS unsigned char* ring, const bf16* x1row, float inv2, const float* nffn, const int* ex, const float* pg, const unsigned char* U6, const unsigned char* V6,
;                    const float* usc, const float* vsc, float* orow, int lane) {
;     ...
;     const float ysc = 1.0f;
;     asm volatile("s_waitcnt vmcnt(0)" ::: "memory");
; #pragma unroll
;     for (int i = 0; i < 16; ++i) {
;         const v2u aw = *(const v2u*)(x1row + i * 256 + lane * 4);
;         *(f32x4*)(orow + i * 256 + lane * 4) = (f32x4){bflo(aw.x) + ysc * y[2 * i].x, bfhi(aw.x) + ysc * y[2 * i].y, bflo(aw.y) + ysc * y[2 * i + 1].x, bfhi(aw.y) + ysc * y[2 * i + 1].y};
;     }
; __global__ void __launch_bounds__(NTHREADS, 2) fwd(Args args) {
;     ...
;             for (int j = 0; j < 4; ++j) { const int t = tb * 32 + wave * 4 + j;
;                 peer_token(lds + wave * (4 * RSLOT), XB + (size_t)t * DM, inv2[t], norm_ffn, experts + (size_t)t * 128, pgates + (size_t)t * 128, U8, V8, usc, vsc, out + (size_t)t * DM, lane); }
.Lpvt9E:
	s_lshl_b32 s46, s76, 1
	s_add_i32 s46, s46, s97
	s_ashr_i32 s47, s46, 31
	s_lshl_b64 s[46:47], s[46:47], 13
	v_lshl_add_u64 v[16:17], v[68:69], 0, s[46:47]
	s_mov_b64 s[46:47], 0x2000
	v_lshl_add_u64 v[2:3], v[16:17], 0, s[46:47]
	s_mov_b64 s[46:47], 0x3000
	v_lshl_add_u64 v[4:5], v[16:17], 0, s[46:47]
	global_load_dwordx2 v[98:99], v[2:3], off
	global_load_dwordx2 v[100:101], v[2:3], off offset:512
	global_load_dwordx2 v[102:103], v[2:3], off offset:1024
	global_load_dwordx2 v[104:105], v[2:3], off offset:1536
	global_load_dwordx2 v[126:127], v[2:3], off offset:2048
	global_load_dwordx2 v[128:129], v[2:3], off offset:2560
	global_load_dwordx2 v[130:131], v[2:3], off offset:3072
	global_load_dwordx2 v[132:133], v[2:3], off offset:3584
	global_load_dwordx2 v[136:137], v[4:5], off
	global_load_dwordx2 v[138:139], v[4:5], off offset:512
	global_load_dwordx2 v[140:141], v[4:5], off offset:1024
	global_load_dwordx2 v[142:143], v[4:5], off offset:1536
	global_load_dwordx2 v[8:9], v[4:5], off offset:2048
	global_load_dwordx2 v[10:11], v[4:5], off offset:2560
	global_load_dwordx2 v[12:13], v[4:5], off offset:3072
	global_load_dwordx2 v[14:15], v[4:5], off offset:3584
	v_lshl_add_u64 v[18:19], s[44:45], 2, v[76:77]
	s_mov_b64 s[46:47], 0x2000
	v_lshl_add_u64 v[6:7], v[18:19], 0, s[46:47]
	s_mov_b64 s[46:47], 0x3000
	v_lshl_add_u64 v[16:17], v[18:19], 0, s[46:47]
	s_mov_b64 s[46:47], 0x4000
	v_lshl_add_u64 v[112:113], v[18:19], 0, s[46:47]
	s_mov_b64 s[46:47], 0x6000
	v_lshl_add_u64 v[242:243], v[18:19], 0, s[46:47]
	s_mov_b64 s[46:47], 0x7000
	v_lshl_add_u64 v[124:125], v[18:19], 0, s[46:47]
	v_lshlrev_b32_e32 v2, 16, v146
	v_and_b32_e32 v3, 0xffff0000, v146
	v_lshlrev_b32_e32 v4, 16, v147
	v_and_b32_e32 v5, 0xffff0000, v147
	v_pk_add_f32 v[2:3], v[94:95], v[2:3]
	v_pk_add_f32 v[4:5], v[96:97], v[4:5]
	global_store_dwordx4 v[18:19], v[2:5], off sc1
	v_lshlrev_b32_e32 v244, 16, v148
	v_and_b32_e32 v245, 0xffff0000, v148
	v_lshlrev_b32_e32 v246, 16, v149
	v_and_b32_e32 v247, 0xffff0000, v149
	v_pk_add_f32 v[244:245], v[92:93], v[244:245]
	v_pk_add_f32 v[246:247], v[90:91], v[246:247]
	global_store_dwordx4 v[18:19], v[244:247], off offset:1024 sc1
	v_lshlrev_b32_e32 v120, 16, v150
	v_and_b32_e32 v121, 0xffff0000, v150
	v_lshlrev_b32_e32 v122, 16, v151
	v_and_b32_e32 v123, 0xffff0000, v151
	v_pk_add_f32 v[120:121], v[88:89], v[120:121]
	v_pk_add_f32 v[122:123], v[86:87], v[122:123]
	global_store_dwordx4 v[18:19], v[120:123], off offset:2048 sc1
	v_lshlrev_b32_e32 v2, 16, v152
	v_and_b32_e32 v3, 0xffff0000, v152
	v_lshlrev_b32_e32 v4, 16, v153
	v_and_b32_e32 v5, 0xffff0000, v153
	v_pk_add_f32 v[2:3], v[84:85], v[2:3]
	v_pk_add_f32 v[4:5], v[82:83], v[4:5]
	global_store_dwordx4 v[18:19], v[2:5], off offset:3072 sc1
	v_lshlrev_b32_e32 v244, 16, v154
	v_and_b32_e32 v245, 0xffff0000, v154
	v_lshlrev_b32_e32 v246, 16, v155
	v_and_b32_e32 v247, 0xffff0000, v155
	v_pk_add_f32 v[244:245], v[64:65], v[244:245]
	v_pk_add_f32 v[246:247], v[80:81], v[246:247]
	global_store_dwordx4 v[6:7], v[244:247], off offset:-4096 sc1
	v_lshlrev_b32_e32 v120, 16, v156
	v_and_b32_e32 v121, 0xffff0000, v156
	v_lshlrev_b32_e32 v122, 16, v157
	v_and_b32_e32 v123, 0xffff0000, v157
	v_pk_add_f32 v[120:121], v[62:63], v[120:121]
	v_pk_add_f32 v[122:123], v[60:61], v[122:123]
	global_store_dwordx4 v[6:7], v[120:123], off offset:-3072 sc1
	v_lshlrev_b32_e32 v2, 16, v158
	v_and_b32_e32 v3, 0xffff0000, v158
	v_lshlrev_b32_e32 v4, 16, v159
	v_and_b32_e32 v5, 0xffff0000, v159
	v_pk_add_f32 v[2:3], v[58:59], v[2:3]
	v_pk_add_f32 v[4:5], v[56:57], v[4:5]
	global_store_dwordx4 v[6:7], v[2:5], off offset:-2048 sc1
	v_lshlrev_b32_e32 v244, 16, v160
	v_and_b32_e32 v245, 0xffff0000, v160
	v_lshlrev_b32_e32 v246, 16, v161
	v_and_b32_e32 v247, 0xffff0000, v161
	v_pk_add_f32 v[244:245], v[54:55], v[244:245]
	v_pk_add_f32 v[246:247], v[52:53], v[246:247]
	global_store_dwordx4 v[6:7], v[244:247], off offset:-1024 sc1
	v_lshlrev_b32_e32 v120, 16, v162
	v_and_b32_e32 v121, 0xffff0000, v162
	v_lshlrev_b32_e32 v122, 16, v163
	v_and_b32_e32 v123, 0xffff0000, v163
	v_pk_add_f32 v[120:121], v[50:51], v[120:121]
	v_pk_add_f32 v[122:123], v[48:49], v[122:123]
	global_store_dwordx4 v[6:7], v[120:123], off sc1
	v_lshlrev_b32_e32 v2, 16, v164
	v_and_b32_e32 v3, 0xffff0000, v164
	v_lshlrev_b32_e32 v4, 16, v165
	v_and_b32_e32 v5, 0xffff0000, v165
	v_pk_add_f32 v[2:3], v[46:47], v[2:3]
	v_pk_add_f32 v[4:5], v[44:45], v[4:5]
	global_store_dwordx4 v[6:7], v[2:5], off offset:1024 sc1
	v_lshlrev_b32_e32 v244, 16, v166
	v_and_b32_e32 v245, 0xffff0000, v166
	v_lshlrev_b32_e32 v246, 16, v167
	v_and_b32_e32 v247, 0xffff0000, v167
	v_pk_add_f32 v[244:245], v[42:43], v[244:245]
	v_pk_add_f32 v[246:247], v[40:41], v[246:247]
	global_store_dwordx4 v[6:7], v[244:247], off offset:2048 sc1
	v_lshlrev_b32_e32 v120, 16, v168
	v_and_b32_e32 v121, 0xffff0000, v168
	v_lshlrev_b32_e32 v122, 16, v169
	v_and_b32_e32 v123, 0xffff0000, v169
	v_pk_add_f32 v[120:121], v[38:39], v[120:121]
	v_pk_add_f32 v[122:123], v[36:37], v[122:123]
	global_store_dwordx4 v[6:7], v[120:123], off offset:3072 sc1
	v_lshlrev_b32_e32 v2, 16, v170
	v_and_b32_e32 v3, 0xffff0000, v170
	v_lshlrev_b32_e32 v4, 16, v171
	v_and_b32_e32 v5, 0xffff0000, v171
	v_pk_add_f32 v[2:3], v[32:33], v[2:3]
	v_pk_add_f32 v[4:5], v[34:35], v[4:5]
	global_store_dwordx4 v[16:17], v[2:5], off sc1
	v_lshlrev_b32_e32 v244, 16, v172
	v_and_b32_e32 v245, 0xffff0000, v172
	v_lshlrev_b32_e32 v246, 16, v173
	v_and_b32_e32 v247, 0xffff0000, v173
	v_pk_add_f32 v[244:245], v[30:31], v[244:245]
	v_pk_add_f32 v[246:247], v[28:29], v[246:247]
	global_store_dwordx4 v[16:17], v[244:247], off offset:1024 sc1
	v_lshlrev_b32_e32 v120, 16, v174
	v_and_b32_e32 v121, 0xffff0000, v174
	v_lshlrev_b32_e32 v122, 16, v175
	v_and_b32_e32 v123, 0xffff0000, v175
	v_pk_add_f32 v[120:121], v[26:27], v[120:121]
	v_pk_add_f32 v[122:123], v[24:25], v[122:123]
	global_store_dwordx4 v[16:17], v[120:123], off offset:2048 sc1
	v_lshlrev_b32_e32 v2, 16, v176
	v_and_b32_e32 v3, 0xffff0000, v176
	v_lshlrev_b32_e32 v4, 16, v177
	v_and_b32_e32 v5, 0xffff0000, v177
	v_pk_add_f32 v[2:3], v[20:21], v[2:3]
	v_pk_add_f32 v[4:5], v[22:23], v[4:5]
	global_store_dwordx4 v[16:17], v[2:5], off offset:3072 sc1
	s_waitcnt vmcnt(31)
; DI void peer_token(LAS unsigned char* ring, const bf16* x1row, float inv2, const float* nffn, const int* ex, const float* pg, const unsigned char* U6, const unsigned char* V6,
;                    const float* usc, const float* vsc, float* orow, int lane) {
;     ...
;     const float ysc = 1.0f;
;     asm volatile("s_waitcnt vmcnt(0)" ::: "memory");
; #pragma unroll
;     for (int i = 0; i < 16; ++i) {
;         const v2u aw = *(const v2u*)(x1row + i * 256 + lane * 4);
;         *(f32x4*)(orow + i * 256 + lane * 4) = (f32x4){bflo(aw.x) + ysc * y[2 * i].x, bfhi(aw.x) + ysc * y[2 * i].y, bflo(aw.y) + ysc * y[2 * i + 1].x, bfhi(aw.y) + ysc * y[2 * i + 1].y};
;     }
	v_lshlrev_b32_e32 v244, 16, v98
	v_and_b32_e32 v245, 0xffff0000, v98
	v_lshlrev_b32_e32 v246, 16, v99
	v_and_b32_e32 v247, 0xffff0000, v99
	v_pk_add_f32 v[244:245], v[178:179], v[244:245]
	v_pk_add_f32 v[246:247], v[180:181], v[246:247]
	global_store_dwordx4 v[112:113], v[244:247], off sc1
	s_waitcnt vmcnt(31)
	v_lshlrev_b32_e32 v120, 16, v100
	v_and_b32_e32 v121, 0xffff0000, v100
	v_lshlrev_b32_e32 v122, 16, v101
	v_and_b32_e32 v123, 0xffff0000, v101
	v_pk_add_f32 v[120:121], v[182:183], v[120:121]
	v_pk_add_f32 v[122:123], v[184:185], v[122:123]
	global_store_dwordx4 v[112:113], v[120:123], off offset:1024 sc1
	s_waitcnt vmcnt(31)
	v_lshlrev_b32_e32 v2, 16, v102
	v_and_b32_e32 v3, 0xffff0000, v102
	v_lshlrev_b32_e32 v4, 16, v103
	v_and_b32_e32 v5, 0xffff0000, v103
	v_pk_add_f32 v[2:3], v[186:187], v[2:3]
	v_pk_add_f32 v[4:5], v[188:189], v[4:5]
	global_store_dwordx4 v[112:113], v[2:5], off offset:2048 sc1
	s_waitcnt vmcnt(31)
	v_lshlrev_b32_e32 v244, 16, v104
	v_and_b32_e32 v245, 0xffff0000, v104
	v_lshlrev_b32_e32 v246, 16, v105
	v_and_b32_e32 v247, 0xffff0000, v105
	v_pk_add_f32 v[244:245], v[190:191], v[244:245]
	v_pk_add_f32 v[246:247], v[192:193], v[246:247]
	global_store_dwordx4 v[112:113], v[244:247], off offset:3072 sc1
	s_waitcnt vmcnt(31)
	v_lshlrev_b32_e32 v120, 16, v126
	v_and_b32_e32 v121, 0xffff0000, v126
	v_lshlrev_b32_e32 v122, 16, v127
	v_and_b32_e32 v123, 0xffff0000, v127
	v_pk_add_f32 v[120:121], v[194:195], v[120:121]
	v_pk_add_f32 v[122:123], v[196:197], v[122:123]
	global_store_dwordx4 v[242:243], v[120:123], off offset:-4096 sc1
	s_waitcnt vmcnt(31)
	v_lshlrev_b32_e32 v2, 16, v128
	v_and_b32_e32 v3, 0xffff0000, v128
	v_lshlrev_b32_e32 v4, 16, v129
	v_and_b32_e32 v5, 0xffff0000, v129
	v_pk_add_f32 v[2:3], v[198:199], v[2:3]
	v_pk_add_f32 v[4:5], v[200:201], v[4:5]
	global_store_dwordx4 v[242:243], v[2:5], off offset:-3072 sc1
	s_waitcnt vmcnt(31)
	v_lshlrev_b32_e32 v244, 16, v130
	v_and_b32_e32 v245, 0xffff0000, v130
	v_lshlrev_b32_e32 v246, 16, v131
	v_and_b32_e32 v247, 0xffff0000, v131
	v_pk_add_f32 v[244:245], v[202:203], v[244:245]
	v_pk_add_f32 v[246:247], v[204:205], v[246:247]
	global_store_dwordx4 v[242:243], v[244:247], off offset:-2048 sc1
	s_waitcnt vmcnt(31)
	v_lshlrev_b32_e32 v120, 16, v132
	v_and_b32_e32 v121, 0xffff0000, v132
	v_lshlrev_b32_e32 v122, 16, v133
	v_and_b32_e32 v123, 0xffff0000, v133
	v_pk_add_f32 v[120:121], v[206:207], v[120:121]
	v_pk_add_f32 v[122:123], v[208:209], v[122:123]
	global_store_dwordx4 v[242:243], v[120:123], off offset:-1024 sc1
	s_waitcnt vmcnt(31)
	v_lshlrev_b32_e32 v2, 16, v136
	v_and_b32_e32 v3, 0xffff0000, v136
	v_lshlrev_b32_e32 v4, 16, v137
	v_and_b32_e32 v5, 0xffff0000, v137
	v_pk_add_f32 v[2:3], v[210:211], v[2:3]
	v_pk_add_f32 v[4:5], v[212:213], v[4:5]
	global_store_dwordx4 v[242:243], v[2:5], off sc1
	s_waitcnt vmcnt(31)
	v_lshlrev_b32_e32 v244, 16, v138
	v_and_b32_e32 v245, 0xffff0000, v138
	v_lshlrev_b32_e32 v246, 16, v139
	v_and_b32_e32 v247, 0xffff0000, v139
	v_pk_add_f32 v[244:245], v[214:215], v[244:245]
	v_pk_add_f32 v[246:247], v[216:217], v[246:247]
	global_store_dwordx4 v[242:243], v[244:247], off offset:1024 sc1
	s_waitcnt vmcnt(31)
	v_lshlrev_b32_e32 v120, 16, v140
	v_and_b32_e32 v121, 0xffff0000, v140
	v_lshlrev_b32_e32 v122, 16, v141
	v_and_b32_e32 v123, 0xffff0000, v141
	v_pk_add_f32 v[120:121], v[218:219], v[120:121]
	v_pk_add_f32 v[122:123], v[220:221], v[122:123]
	global_store_dwordx4 v[242:243], v[120:123], off offset:2048 sc1
	s_waitcnt vmcnt(31)
	v_lshlrev_b32_e32 v2, 16, v142
	v_and_b32_e32 v3, 0xffff0000, v142
	v_lshlrev_b32_e32 v4, 16, v143
	v_and_b32_e32 v5, 0xffff0000, v143
	v_pk_add_f32 v[2:3], v[222:223], v[2:3]
	v_pk_add_f32 v[4:5], v[224:225], v[4:5]
	global_store_dwordx4 v[242:243], v[2:5], off offset:3072 sc1
	s_waitcnt vmcnt(31)
	v_lshlrev_b32_e32 v244, 16, v8
	v_and_b32_e32 v245, 0xffff0000, v8
	v_lshlrev_b32_e32 v246, 16, v9
	v_and_b32_e32 v247, 0xffff0000, v9
	v_pk_add_f32 v[244:245], v[226:227], v[244:245]
	v_pk_add_f32 v[246:247], v[228:229], v[246:247]
	global_store_dwordx4 v[124:125], v[244:247], off sc1
	s_waitcnt vmcnt(31)
	v_lshlrev_b32_e32 v120, 16, v10
	v_and_b32_e32 v121, 0xffff0000, v10
	v_lshlrev_b32_e32 v122, 16, v11
	v_and_b32_e32 v123, 0xffff0000, v11
	v_pk_add_f32 v[120:121], v[230:231], v[120:121]
	v_pk_add_f32 v[122:123], v[232:233], v[122:123]
	global_store_dwordx4 v[124:125], v[120:123], off offset:1024 sc1
	s_waitcnt vmcnt(31)
	v_lshlrev_b32_e32 v2, 16, v12
	v_and_b32_e32 v3, 0xffff0000, v12
	v_lshlrev_b32_e32 v4, 16, v13
	v_and_b32_e32 v5, 0xffff0000, v13
	v_pk_add_f32 v[2:3], v[234:235], v[2:3]
	v_pk_add_f32 v[4:5], v[236:237], v[4:5]
	global_store_dwordx4 v[124:125], v[2:5], off offset:2048 sc1
	s_waitcnt vmcnt(31)
	v_lshlrev_b32_e32 v244, 16, v14
	v_and_b32_e32 v245, 0xffff0000, v14
	v_lshlrev_b32_e32 v246, 16, v15
	v_and_b32_e32 v247, 0xffff0000, v15
	v_pk_add_f32 v[244:245], v[238:239], v[244:245]
	v_pk_add_f32 v[246:247], v[240:241], v[246:247]
	global_store_dwordx4 v[124:125], v[244:247], off offset:3072 sc1
	s_add_i32 s76, s76, 1
	s_cmp_eq_u32 s76, 2
	s_cbranch_scc0 .LBB0_901
	s_add_i32 s2, s2, s3
	s_cmpk_gt_i32 s2, 0xff
	s_barrier
	s_cbranch_scc0 .LBB0_892
